# k_agg1: final step of a wave gathers only 2/4/6 rows when no active node has more neighbours left (pad terms of the fp16 tree omitted)
# speedup vs baseline: 1.0127x; 1.0031x over previous
.LBB3_4:
	v_sub_u32_e32 v62, v1, v0
	v_cmp_lt_i32_e64 s[18:19], 6, v62
	s_cmp_eq_u64 s[18:19], 0
	s_cbranch_scc0 .Lagg_full
	v_cmp_lt_i32_e64 s[18:19], 4, v62
	s_cmp_eq_u64 s[18:19], 0
	s_cbranch_scc0 .Lagg_six
	v_cmp_lt_i32_e64 s[18:19], 2, v62
	s_cmp_eq_u64 s[18:19], 0
	s_cbranch_scc0 .Lagg_four
	s_branch .Lagg_two
.Lagg_full:
	global_load_dwordx4 v[30:33], v[2:3], off
	v_add_u32_e32 v0, 8, v0
	v_cmp_ge_i32_e64 s[18:19], v0, v1
	v_lshl_add_u64 v[2:3], v[2:3], 0, 16
	s_or_b64 s[30:31], s[18:19], s[30:31]
	s_waitcnt vmcnt(0)
	v_lshlrev_b32_sdwa v34, v28, v30 dst_sel:DWORD dst_unused:UNUSED_PAD src0_sel:DWORD src1_sel:WORD_1
	v_lshlrev_b32_sdwa v30, v28, v30 dst_sel:DWORD dst_unused:UNUSED_PAD src0_sel:DWORD src1_sel:WORD_0
	v_lshlrev_b32_sdwa v35, v28, v31 dst_sel:DWORD dst_unused:UNUSED_PAD src0_sel:DWORD src1_sel:WORD_1
	v_lshlrev_b32_sdwa v31, v28, v31 dst_sel:DWORD dst_unused:UNUSED_PAD src0_sel:DWORD src1_sel:WORD_0
	v_lshlrev_b32_sdwa v36, v28, v32 dst_sel:DWORD dst_unused:UNUSED_PAD src0_sel:DWORD src1_sel:WORD_1
	v_lshlrev_b32_sdwa v32, v28, v32 dst_sel:DWORD dst_unused:UNUSED_PAD src0_sel:DWORD src1_sel:WORD_0
	v_lshlrev_b32_sdwa v37, v28, v33 dst_sel:DWORD dst_unused:UNUSED_PAD src0_sel:DWORD src1_sel:WORD_1
	v_lshlrev_b32_sdwa v33, v28, v33 dst_sel:DWORD dst_unused:UNUSED_PAD src0_sel:DWORD src1_sel:WORD_0
	v_or_b32_e32 v38, v34, v7
	v_or_b32_e32 v39, v30, v6
	v_or_b32_e32 v42, v35, v7
	v_or_b32_e32 v40, v31, v6
	v_or_b32_e32 v50, v36, v7
	v_or_b32_e32 v46, v32, v6
	v_or_b32_e32 v58, v37, v7
	v_or_b32_e32 v54, v33, v6
	global_load_dwordx4 v[30:33], v39, s[20:21]
	global_load_dwordx4 v[34:37], v38, s[20:21]
	s_nop 0
	global_load_dwordx4 v[38:41], v40, s[20:21]
	s_nop 0
	global_load_dwordx4 v[42:45], v42, s[20:21]
	s_nop 0
	global_load_dwordx4 v[46:49], v46, s[20:21]
	s_nop 0
	global_load_dwordx4 v[50:53], v50, s[20:21]
	s_nop 0
	global_load_dwordx4 v[54:57], v54, s[20:21]
	s_nop 0
	global_load_dwordx4 v[58:61], v58, s[20:21]
	s_waitcnt vmcnt(6)
	v_pk_add_f16 v33, v33, v37
	v_pk_add_f16 v32, v32, v36
	v_pk_add_f16 v31, v31, v35
	v_pk_add_f16 v30, v30, v34
	s_waitcnt vmcnt(4)
	v_pk_add_f16 v34, v41, v45
	v_pk_add_f16 v35, v40, v44
	v_pk_add_f16 v36, v39, v43
	v_pk_add_f16 v37, v38, v42
	s_waitcnt vmcnt(2)
	v_pk_add_f16 v38, v49, v53
	v_pk_add_f16 v39, v48, v52
	v_pk_add_f16 v40, v47, v51
	v_pk_add_f16 v41, v46, v50
	s_waitcnt vmcnt(0)
	v_pk_add_f16 v42, v57, v61
	v_pk_add_f16 v43, v56, v60
	v_pk_add_f16 v44, v55, v59
	v_pk_add_f16 v45, v54, v58
	v_pk_add_f16 v30, v30, v37
	v_pk_add_f16 v31, v31, v36
	v_pk_add_f16 v32, v32, v35
	v_pk_add_f16 v33, v33, v34
	v_pk_add_f16 v34, v41, v45
	v_pk_add_f16 v35, v40, v44
	v_pk_add_f16 v36, v39, v43
	v_pk_add_f16 v37, v38, v42
	v_pk_add_f16 v36, v32, v36
	v_pk_add_f16 v37, v33, v37
	v_pk_add_f16 v33, v31, v35
	v_pk_add_f16 v31, v30, v34
	v_cvt_f32_f16_e32 v32, v33
	v_cvt_f32_f16_e32 v30, v31
	v_cvt_f32_f16_sdwa v31, v31 dst_sel:DWORD dst_unused:UNUSED_PAD src0_sel:WORD_1
	v_cvt_f32_f16_sdwa v33, v33 dst_sel:DWORD dst_unused:UNUSED_PAD src0_sel:WORD_1
	v_cvt_f32_f16_e32 v34, v36
	v_cvt_f32_f16_sdwa v35, v36 dst_sel:DWORD dst_unused:UNUSED_PAD src0_sel:WORD_1
	v_cvt_f32_f16_e32 v36, v37
	v_cvt_f32_f16_sdwa v37, v37 dst_sel:DWORD dst_unused:UNUSED_PAD src0_sel:WORD_1
	v_pk_add_f32 v[18:19], v[18:19], v[30:31]
	v_pk_add_f32 v[16:17], v[16:17], v[32:33]
	v_pk_add_f32 v[14:15], v[14:15], v[34:35]
	v_pk_add_f32 v[12:13], v[12:13], v[36:37]
	s_andn2_b64 exec, exec, s[30:31]
	s_cbranch_execnz .LBB3_4
	s_branch .Lagg_loop_done
.Lagg_two:
	global_load_dword v30, v[2:3], off
	s_waitcnt vmcnt(0)
	v_lshlrev_b32_sdwa v34, v28, v30 dst_sel:DWORD dst_unused:UNUSED_PAD src0_sel:DWORD src1_sel:WORD_1
	v_lshlrev_b32_sdwa v30, v28, v30 dst_sel:DWORD dst_unused:UNUSED_PAD src0_sel:DWORD src1_sel:WORD_0
	v_or_b32_e32 v39, v30, v6
	v_or_b32_e32 v38, v34, v7
	global_load_dwordx4 v[30:33], v39, s[20:21]
	s_nop 0
	global_load_dwordx4 v[34:37], v38, s[20:21]
	s_nop 0
	s_waitcnt vmcnt(0)
	v_pk_add_f16 v33, v33, v37
	v_pk_add_f16 v32, v32, v36
	v_pk_add_f16 v31, v31, v35
	v_pk_add_f16 v30, v30, v34
	v_cvt_f32_f16_e32 v54, v30
	v_cvt_f32_f16_sdwa v55, v30 dst_sel:DWORD dst_unused:UNUSED_PAD src0_sel:WORD_1
	v_cvt_f32_f16_e32 v56, v31
	v_cvt_f32_f16_sdwa v57, v31 dst_sel:DWORD dst_unused:UNUSED_PAD src0_sel:WORD_1
	v_cvt_f32_f16_e32 v58, v32
	v_cvt_f32_f16_sdwa v59, v32 dst_sel:DWORD dst_unused:UNUSED_PAD src0_sel:WORD_1
	v_cvt_f32_f16_e32 v60, v33
	v_cvt_f32_f16_sdwa v61, v33 dst_sel:DWORD dst_unused:UNUSED_PAD src0_sel:WORD_1
	v_pk_add_f32 v[18:19], v[18:19], v[54:55]
	v_pk_add_f32 v[16:17], v[16:17], v[56:57]
	v_pk_add_f32 v[14:15], v[14:15], v[58:59]
	v_pk_add_f32 v[12:13], v[12:13], v[60:61]
	s_branch .Lagg_loop_done
.Lagg_four:
	global_load_dwordx2 v[30:31], v[2:3], off
	s_waitcnt vmcnt(0)
	v_lshlrev_b32_sdwa v34, v28, v30 dst_sel:DWORD dst_unused:UNUSED_PAD src0_sel:DWORD src1_sel:WORD_1
	v_lshlrev_b32_sdwa v30, v28, v30 dst_sel:DWORD dst_unused:UNUSED_PAD src0_sel:DWORD src1_sel:WORD_0
	v_lshlrev_b32_sdwa v35, v28, v31 dst_sel:DWORD dst_unused:UNUSED_PAD src0_sel:DWORD src1_sel:WORD_1
	v_lshlrev_b32_sdwa v31, v28, v31 dst_sel:DWORD dst_unused:UNUSED_PAD src0_sel:DWORD src1_sel:WORD_0
	v_or_b32_e32 v39, v30, v6
	v_or_b32_e32 v38, v34, v7
	v_or_b32_e32 v40, v31, v6
	v_or_b32_e32 v42, v35, v7
	global_load_dwordx4 v[30:33], v39, s[20:21]
	s_nop 0
	global_load_dwordx4 v[34:37], v38, s[20:21]
	s_nop 0
	global_load_dwordx4 v[38:41], v40, s[20:21]
	s_nop 0
	global_load_dwordx4 v[42:45], v42, s[20:21]
	s_nop 0
	s_waitcnt vmcnt(2)
	v_pk_add_f16 v33, v33, v37
	v_pk_add_f16 v32, v32, v36
	v_pk_add_f16 v31, v31, v35
	v_pk_add_f16 v30, v30, v34
	s_waitcnt vmcnt(0)
	v_pk_add_f16 v34, v41, v45
	v_pk_add_f16 v35, v40, v44
	v_pk_add_f16 v36, v39, v43
	v_pk_add_f16 v37, v38, v42
	v_pk_add_f16 v30, v30, v37
	v_pk_add_f16 v31, v31, v36
	v_pk_add_f16 v32, v32, v35
	v_pk_add_f16 v33, v33, v34
	v_cvt_f32_f16_e32 v54, v30
	v_cvt_f32_f16_sdwa v55, v30 dst_sel:DWORD dst_unused:UNUSED_PAD src0_sel:WORD_1
	v_cvt_f32_f16_e32 v56, v31
	v_cvt_f32_f16_sdwa v57, v31 dst_sel:DWORD dst_unused:UNUSED_PAD src0_sel:WORD_1
	v_cvt_f32_f16_e32 v58, v32
	v_cvt_f32_f16_sdwa v59, v32 dst_sel:DWORD dst_unused:UNUSED_PAD src0_sel:WORD_1
	v_cvt_f32_f16_e32 v60, v33
	v_cvt_f32_f16_sdwa v61, v33 dst_sel:DWORD dst_unused:UNUSED_PAD src0_sel:WORD_1
	v_pk_add_f32 v[18:19], v[18:19], v[54:55]
	v_pk_add_f32 v[16:17], v[16:17], v[56:57]
	v_pk_add_f32 v[14:15], v[14:15], v[58:59]
	v_pk_add_f32 v[12:13], v[12:13], v[60:61]
	s_branch .Lagg_loop_done
.Lagg_six:
	global_load_dwordx3 v[30:32], v[2:3], off
	s_waitcnt vmcnt(0)
	v_lshlrev_b32_sdwa v34, v28, v30 dst_sel:DWORD dst_unused:UNUSED_PAD src0_sel:DWORD src1_sel:WORD_1
	v_lshlrev_b32_sdwa v30, v28, v30 dst_sel:DWORD dst_unused:UNUSED_PAD src0_sel:DWORD src1_sel:WORD_0
	v_lshlrev_b32_sdwa v35, v28, v31 dst_sel:DWORD dst_unused:UNUSED_PAD src0_sel:DWORD src1_sel:WORD_1
	v_lshlrev_b32_sdwa v31, v28, v31 dst_sel:DWORD dst_unused:UNUSED_PAD src0_sel:DWORD src1_sel:WORD_0
	v_lshlrev_b32_sdwa v36, v28, v32 dst_sel:DWORD dst_unused:UNUSED_PAD src0_sel:DWORD src1_sel:WORD_1
	v_lshlrev_b32_sdwa v32, v28, v32 dst_sel:DWORD dst_unused:UNUSED_PAD src0_sel:DWORD src1_sel:WORD_0
	v_or_b32_e32 v39, v30, v6
	v_or_b32_e32 v38, v34, v7
	v_or_b32_e32 v40, v31, v6
	v_or_b32_e32 v42, v35, v7
	v_or_b32_e32 v46, v32, v6
	v_or_b32_e32 v50, v36, v7
	global_load_dwordx4 v[30:33], v39, s[20:21]
	s_nop 0
	global_load_dwordx4 v[34:37], v38, s[20:21]
	s_nop 0
	global_load_dwordx4 v[38:41], v40, s[20:21]
	s_nop 0
	global_load_dwordx4 v[42:45], v42, s[20:21]
	s_nop 0
	global_load_dwordx4 v[46:49], v46, s[20:21]
	s_nop 0
	global_load_dwordx4 v[50:53], v50, s[20:21]
	s_nop 0
	s_waitcnt vmcnt(4)
	v_pk_add_f16 v33, v33, v37
	v_pk_add_f16 v32, v32, v36
	v_pk_add_f16 v31, v31, v35
	v_pk_add_f16 v30, v30, v34
	s_waitcnt vmcnt(2)
	v_pk_add_f16 v34, v41, v45
	v_pk_add_f16 v35, v40, v44
	v_pk_add_f16 v36, v39, v43
	v_pk_add_f16 v37, v38, v42
	v_pk_add_f16 v30, v30, v37
	v_pk_add_f16 v31, v31, v36
	v_pk_add_f16 v32, v32, v35
	v_pk_add_f16 v33, v33, v34
	s_waitcnt vmcnt(0)
	v_pk_add_f16 v38, v49, v53
	v_pk_add_f16 v39, v48, v52
	v_pk_add_f16 v40, v47, v51
	v_pk_add_f16 v41, v46, v50
	v_pk_add_f16 v30, v30, v41
	v_pk_add_f16 v31, v31, v40
	v_pk_add_f16 v32, v32, v39
	v_pk_add_f16 v33, v33, v38
	v_cvt_f32_f16_e32 v54, v30
	v_cvt_f32_f16_sdwa v55, v30 dst_sel:DWORD dst_unused:UNUSED_PAD src0_sel:WORD_1
	v_cvt_f32_f16_e32 v56, v31
	v_cvt_f32_f16_sdwa v57, v31 dst_sel:DWORD dst_unused:UNUSED_PAD src0_sel:WORD_1
	v_cvt_f32_f16_e32 v58, v32
	v_cvt_f32_f16_sdwa v59, v32 dst_sel:DWORD dst_unused:UNUSED_PAD src0_sel:WORD_1
	v_cvt_f32_f16_e32 v60, v33
	v_cvt_f32_f16_sdwa v61, v33 dst_sel:DWORD dst_unused:UNUSED_PAD src0_sel:WORD_1
	v_pk_add_f32 v[18:19], v[18:19], v[54:55]
	v_pk_add_f32 v[16:17], v[16:17], v[56:57]
	v_pk_add_f32 v[14:15], v[14:15], v[58:59]
	v_pk_add_f32 v[12:13], v[12:13], v[60:61]
	s_branch .Lagg_loop_done
